# P2 norm->fp8: scale/shift quads loaded once before the row loop, next row's x loads issued one row ahead (second register set)
# speedup vs baseline: 1.0063x; 1.0063x over previous
; #define FRESH(F) do { (F).tid = ltid(); (F).lane = (F).tid & 63; (F).wave = __builtin_amdgcn_readfirstlane((F).tid >> 6); (F).ka = fresh_karg(); (F).ws = (unsigned char*)(GAS unsigned char*)(F).ka[25]; (F).ctl = (unsigned*)(F).ws; } while (0)
; #define SEAM(k) do { if (IN(k) && IN((k) + 1)) xcd_barrier(bar); } while (0)
; #define REP(k) for (int rep_ = 0; rep_ < ((PROBE_REPEAT == (k) || ((k) < 32 && ((PROBE_MASK >> (k)) & 1))) ? 2 : 1); ++rep_)
; #define modv WSP(float, WS_MODV)
; __device__ __forceinline__ void norm_mod_row_f8(const float* xrow, const float* A, const float* B, unsigned char* orow, int lane) {
;     const unsigned l32 = (unsigned)lane * 32u, l8 = (unsigned)lane * 8u;
;     f32x4 v[8]; float s = 0.f;
; #pragma unroll
;     for (int j = 0; j < 4; ++j) { v[2 * j] = *(const f32x4*)((const char*)(xrow + 512 * j) + l32); v[2 * j + 1] = *(const f32x4*)((const char*)(xrow + 512 * j + 4) + l32); }
; #pragma unroll
;     for (int j = 0; j < 8; ++j) s += (v[j].x * v[j].x + v[j].y * v[j].y) + (v[j].z * v[j].z + v[j].w * v[j].w);
;     const float rstd = 1.f / sqrtf(wave_sum(s) * (1.f / DM) + EPS_);
; #pragma unroll
;     for (int j = 0; j < 4; ++j) {
;         const f32x4 a0 = *(const f32x4*)((const char*)(A + 512 * j) + l32), a1 = *(const f32x4*)((const char*)(A + 512 * j + 4) + l32);
;         const f32x4 b0 = *(const f32x4*)((const char*)(B + 512 * j) + l32), b1 = *(const f32x4*)((const char*)(B + 512 * j + 4) + l32);
; __global__ void __launch_bounds__(NWAVES * 64, 2) mk_fwd(Args args) {
;     ...
;     if (IN(2)) REP(2) { FRESH(F); const int gw = F.bid * NWAVES + F.wave; for (int t = gw; t < S_; t += NGW) { if (PROJ_F8) { norm_mod_row_f8(INF(I_X) + (size_t)t * DM, modv, modv + 2048, WSP(unsigned char, WS_H8) + (size_t)t * DM, F.lane); if (PROJ_F8 >= 2) norm_mod_row(INF(I_X) + (size_t)t * DM, modv, modv + 2048, WSP(bf16_t, WS_H) + (size_t)t * DM, F.lane); } else norm_mod_row(INF(I_X) + (size_t)t * DM, modv, modv + 2048, WSP(bf16_t, WS_H) + (size_t)t * DM, F.lane); } } SEAM(2);
.LBB0_198:
	s_cmp_lt_i32 s28, 3
	s_cselect_b64 s[6:7], -1, 0
	s_and_b64 s[6:7], s[6:7], s[4:5]
	s_andn2_b64 vcc, exec, s[6:7]
	s_cbranch_vccnz .LBB0_202
	v_mov_b32_e32 v1, v0
	s_lshl_b32 s8, s2, 3
	v_readfirstlane_b32 s4, v1
	s_ashr_i32 s9, s4, 6
	s_add_i32 s8, s9, s8
	s_mov_b64 s[4:5], s[0:1]
	s_cmpk_gt_i32 s8, 0x3fff
	s_cbranch_scc1 .LBB0_202
	v_and_b32_e32 v1, 63, v1
	v_lshlrev_b32_e32 v2, 5, v1
	v_lshlrev_b32_e32 v4, 3, v1
	v_mbcnt_lo_u32_b32 v1, -1, 0
	v_mbcnt_hi_u32_b32 v5, -1, v1
	v_and_b32_e32 v1, 64, v5
	v_add_u32_e32 v6, 64, v1
	v_xor_b32_e32 v1, 1, v5
	v_cmp_lt_i32_e32 vcc, v1, v6
	v_xor_b32_e32 v7, 2, v5
	s_waitcnt lgkmcnt(0)
	s_load_dwordx2 s[10:11], s[4:5], 0xc8
	s_load_dwordx2 s[12:13], s[4:5], 0x0
	v_cndmask_b32_e32 v1, v5, v1, vcc
	v_cmp_lt_i32_e32 vcc, v7, v6
	v_mov_b32_e32 v3, 0
	s_mov_b64 s[4:5], 0x100000
	v_cndmask_b32_e32 v7, v5, v7, vcc
	v_lshlrev_b32_e32 v54, 2, v7
	v_xor_b32_e32 v7, 4, v5
	v_cmp_lt_i32_e32 vcc, v7, v6
	s_ashr_i32 s9, s8, 31
	v_lshlrev_b32_e32 v1, 2, v1
	v_cndmask_b32_e32 v7, v5, v7, vcc
	v_lshlrev_b32_e32 v55, 2, v7
	v_xor_b32_e32 v7, 8, v5
	v_cmp_lt_i32_e32 vcc, v7, v6
	v_mov_b32_e32 v59, 0x358637bd
	v_mov_b32_e32 v60, 0x260
	v_cndmask_b32_e32 v7, v5, v7, vcc
	v_lshlrev_b32_e32 v56, 2, v7
	v_xor_b32_e32 v7, 16, v5
	v_cmp_lt_i32_e32 vcc, v7, v6
	s_mov_b32 s14, 0xc3e00000
	v_mov_b32_e32 v61, 0x43e00000
	v_cndmask_b32_e32 v7, v5, v7, vcc
	v_lshlrev_b32_e32 v57, 2, v7
	v_xor_b32_e32 v7, 32, v5
	v_cmp_lt_i32_e32 vcc, v7, v6
	s_nop 1
	v_cndmask_b32_e32 v5, v5, v7, vcc
	s_waitcnt lgkmcnt(0)
	v_lshl_add_u64 v[6:7], s[10:11], 0, v[2:3]
	v_lshl_add_u64 v[34:35], v[6:7], 0, s[4:5]
	s_mov_b64 s[4:5], 0x102000
	v_lshl_add_u64 v[36:37], v[6:7], 0, s[4:5]
	s_mov_b64 s[4:5], 0x100800
	v_lshl_add_u64 v[38:39], v[6:7], 0, s[4:5]
	s_mov_b64 s[4:5], 0x102800
	v_lshl_add_u64 v[40:41], v[6:7], 0, s[4:5]
	s_mov_b64 s[4:5], 0x101000
	v_lshl_add_u64 v[42:43], v[6:7], 0, s[4:5]
	s_mov_b64 s[4:5], 0x103000
	v_lshl_add_u64 v[44:45], v[6:7], 0, s[4:5]
	s_mov_b64 s[4:5], 0x101800
	v_lshl_add_u64 v[46:47], v[6:7], 0, s[4:5]
	s_mov_b64 s[4:5], 0x103800
	v_lshl_add_u64 v[48:49], v[6:7], 0, s[4:5]
	s_lshl_b64 s[4:5], s[8:9], 11
	s_add_u32 s4, s10, s4
	v_lshlrev_b32_e32 v58, 2, v5
	v_mov_b32_e32 v5, v3
	s_addc_u32 s5, s11, s5
	v_lshl_add_u64 v[4:5], s[4:5], 0, v[4:5]
	s_mov_b64 s[4:5], 0x2b700000
	s_ashr_i32 s27, s26, 31
	v_lshl_add_u64 v[50:51], v[4:5], 0, s[4:5]
	s_lshl_b64 s[10:11], s[26:27], 11
	s_lshl_b64 s[4:5], s[8:9], 13
	s_add_u32 s4, s12, s4
	s_addc_u32 s5, s13, s5
	v_lshl_add_u64 v[2:3], s[4:5], 0, v[2:3]
	s_mov_b64 s[4:5], 0x1000
	v_lshl_add_u64 v[52:53], v[2:3], 0, s[4:5]
	s_lshl_b64 s[12:13], s[26:27], 13
	s_mov_b32 s9, 0xf800000
	global_load_dwordx4 v[120:123], v[34:35], off
	global_load_dwordx4 v[124:127], v[34:35], off offset:16
	global_load_dwordx4 v[128:131], v[36:37], off
	global_load_dwordx4 v[132:135], v[36:37], off offset:16
	global_load_dwordx4 v[136:139], v[40:41], off
	global_load_dwordx4 v[140:143], v[38:39], off
	global_load_dwordx4 v[144:147], v[38:39], off offset:16
	global_load_dwordx4 v[148:151], v[40:41], off offset:16
	global_load_dwordx4 v[152:155], v[44:45], off
	global_load_dwordx4 v[156:159], v[42:43], off
	global_load_dwordx4 v[160:163], v[42:43], off offset:16
	global_load_dwordx4 v[164:167], v[44:45], off offset:16
	global_load_dwordx4 v[168:171], v[48:49], off
	global_load_dwordx4 v[172:175], v[46:47], off
	global_load_dwordx4 v[176:179], v[46:47], off offset:16
	global_load_dwordx4 v[180:183], v[48:49], off offset:16
	global_load_dwordx4 v[202:205], v[52:53], off offset:-4096
	global_load_dwordx4 v[206:209], v[52:53], off offset:-4080
	global_load_dwordx4 v[210:213], v[52:53], off offset:-2048
	global_load_dwordx4 v[214:217], v[52:53], off
	global_load_dwordx4 v[218:221], v[52:53], off offset:-2032
	global_load_dwordx4 v[222:225], v[52:53], off offset:16
	global_load_dwordx4 v[226:229], v[52:53], off offset:2064
	global_load_dwordx4 v[230:233], v[52:53], off offset:2048
	s_waitcnt vmcnt(0)
	s_branch .Lmy_p2_in
.LBB0_201:
	s_waitcnt vmcnt(4)
.Lmy_p2_in:
	v_mov_b32_e32 v30, v202
	v_mov_b32_e32 v31, v203
	v_mov_b32_e32 v32, v204
	v_mov_b32_e32 v33, v205
	v_mov_b32_e32 v26, v206
	v_mov_b32_e32 v27, v207
	v_mov_b32_e32 v28, v208
	v_mov_b32_e32 v29, v209
	v_mov_b32_e32 v18, v210
	v_mov_b32_e32 v19, v211
	v_mov_b32_e32 v20, v212
	v_mov_b32_e32 v21, v213
	v_mov_b32_e32 v14, v214
	v_mov_b32_e32 v15, v215
	v_mov_b32_e32 v16, v216
	v_mov_b32_e32 v17, v217
	v_mov_b32_e32 v22, v218
	v_mov_b32_e32 v23, v219
	v_mov_b32_e32 v24, v220
	v_mov_b32_e32 v25, v221
	v_mov_b32_e32 v10, v222
	v_mov_b32_e32 v11, v223
	v_mov_b32_e32 v12, v224
	v_mov_b32_e32 v13, v225
	v_mov_b32_e32 v2, v226
	v_mov_b32_e32 v3, v227
	v_mov_b32_e32 v4, v228
	v_mov_b32_e32 v5, v229
	v_mov_b32_e32 v6, v230
	v_mov_b32_e32 v7, v231
	v_mov_b32_e32 v8, v232
	v_mov_b32_e32 v9, v233
	v_mov_b32_e32 v78, 0
	v_mov_b32_e32 v79, 0
	s_add_i32 s8, s8, s26
	v_lshl_add_u64 v[52:53], v[52:53], 0, s[12:13]
	s_cmpk_lt_i32 s8, 0x4000
	s_cbranch_scc0 .Lmy_p2_nopf
	global_load_dwordx4 v[202:205], v[52:53], off offset:-4096
	global_load_dwordx4 v[206:209], v[52:53], off offset:-4080
	global_load_dwordx4 v[210:213], v[52:53], off offset:-2048
	global_load_dwordx4 v[214:217], v[52:53], off
	global_load_dwordx4 v[218:221], v[52:53], off offset:-2032
	global_load_dwordx4 v[222:225], v[52:53], off offset:16
	global_load_dwordx4 v[226:229], v[52:53], off offset:2064
	global_load_dwordx4 v[230:233], v[52:53], off offset:2048
; __device__ __forceinline__ void norm_mod_row_f8(const float* xrow, const float* A, const float* B, unsigned char* orow, int lane) {
;     ...
;     for (int j = 0; j < 4; ++j) { v[2 * j] = *(const f32x4*)((const char*)(xrow + 512 * j) + l32); v[2 * j + 1] = *(const f32x4*)((const char*)(xrow + 512 * j + 4) + l32); }
; #pragma unroll
;     for (int j = 0; j < 8; ++j) s += (v[j].x * v[j].x + v[j].y * v[j].y) + (v[j].z * v[j].z + v[j].w * v[j].w);
;     const float rstd = 1.f / sqrtf(wave_sum(s) * (1.f / DM) + EPS_);
.Lmy_p2_nopf:
	v_mov_b32_e32 v82, v31
	v_mov_b32_e32 v83, v27
	v_mov_b32_e32 v86, v33
	v_mov_b32_e32 v87, v29
	v_mov_b32_e32 v80, v30
	v_mov_b32_e32 v81, v26
	v_mov_b32_e32 v84, v32
	v_mov_b32_e32 v85, v28
	v_pk_mul_f32 v[88:89], v[20:21], v[20:21]
	v_pk_mul_f32 v[90:91], v[18:19], v[18:19]
	v_pk_mul_f32 v[82:83], v[82:83], v[82:83]
	v_pk_mul_f32 v[86:87], v[86:87], v[86:87]
	v_pk_mov_b32 v[104:105], v[90:91], v[88:89] op_sel:[1,0]
	v_mov_b32_e32 v91, v89
	v_pk_fma_f32 v[80:81], v[80:81], v[80:81], v[82:83]
	v_pk_fma_f32 v[82:83], v[84:85], v[84:85], v[86:87]
	v_mul_f32_e32 v92, v23, v23
	v_mul_f32_e32 v94, v25, v25
	v_pk_add_f32 v[84:85], v[104:105], v[90:91]
	v_pk_add_f32 v[80:81], v[80:81], v[82:83]
	v_mul_f32_e32 v103, v14, v14
	v_mul_f32_e32 v106, v15, v15
	v_mul_f32_e32 v107, v16, v16
	v_mul_f32_e32 v108, v17, v17
	v_pk_fma_f32 v[88:89], v[22:23], v[22:23], v[92:93] op_sel_hi:[1,1,0]
	v_pk_fma_f32 v[92:93], v[24:25], v[24:25], v[94:95] op_sel_hi:[1,1,0]
	v_pk_add_f32 v[82:83], v[84:85], v[84:85] op_sel:[0,1] op_sel_hi:[1,0]
	v_pk_add_f32 v[80:81], v[80:81], v[80:81] op_sel:[0,1] op_sel_hi:[1,0]
	v_pk_mul_f32 v[96:97], v[12:13], v[12:13]
	v_pk_mul_f32 v[98:99], v[10:11], v[10:11]
	v_mov_b32_e32 v89, v107
	v_mov_b32_e32 v93, v108
	v_mov_b32_e32 v83, v106
	v_mov_b32_e32 v81, v103
	v_pk_mov_b32 v[94:95], v[98:99], v[96:97] op_sel:[1,0]
	v_mov_b32_e32 v99, v97
	v_pk_add_f32 v[84:85], v[88:89], v[92:93]
	v_pk_add_f32 v[80:81], v[80:81], v[82:83]
	v_mul_f32_e32 v100, v7, v7
	v_mul_f32_e32 v102, v9, v9
	v_pk_add_f32 v[86:87], v[94:95], v[98:99]
	v_pk_add_f32 v[80:81], v[80:81], v[84:85]
	v_mul_f32_e32 v109, v2, v2
	v_mul_f32_e32 v110, v3, v3
	v_mul_f32_e32 v111, v4, v4
	v_mul_f32_e32 v112, v5, v5
	v_pk_fma_f32 v[96:97], v[6:7], v[6:7], v[100:101] op_sel_hi:[1,1,0]
	v_pk_fma_f32 v[100:101], v[8:9], v[8:9], v[102:103] op_sel_hi:[1,1,0]
	v_pk_add_f32 v[86:87], v[86:87], v[86:87] op_sel:[0,1] op_sel_hi:[1,0]
	v_pk_add_f32 v[80:81], v[80:81], v[80:81] op_sel:[0,1] op_sel_hi:[1,0]
	v_mov_b32_e32 v97, v111
	v_mov_b32_e32 v101, v112
	v_mov_b32_e32 v87, v110
	v_mov_b32_e32 v81, v109
	v_pk_add_f32 v[88:89], v[96:97], v[100:101]
	v_pk_add_f32 v[80:81], v[80:81], v[86:87]
	s_nop 0
	v_pk_add_f32 v[80:81], v[80:81], v[88:89]
	s_nop 0
	v_add_f32_e32 v80, v80, v81
	s_waitcnt lgkmcnt(0)
	s_nop 1
	v_add_f32_dpp v80, v80, v80 quad_perm:[1,0,3,2] row_mask:0xf bank_mask:0xf bound_ctrl:1
	s_waitcnt lgkmcnt(0)
	s_nop 1
	v_add_f32_dpp v80, v80, v80 quad_perm:[2,3,0,1] row_mask:0xf bank_mask:0xf bound_ctrl:1
	s_waitcnt lgkmcnt(0)
	s_nop 1
	v_add_f32_dpp v80, v80, v80 row_half_mirror row_mask:0xf bank_mask:0xf bound_ctrl:1
	s_waitcnt lgkmcnt(0)
	s_nop 1
	v_add_f32_dpp v80, v80, v80 row_mirror row_mask:0xf bank_mask:0xf bound_ctrl:1
	ds_bpermute_b32 v81, v57, v80
	s_waitcnt lgkmcnt(0)
	v_add_f32_e32 v80, v80, v81
	ds_bpermute_b32 v81, v58, v80
	s_waitcnt lgkmcnt(0)
; __device__ __forceinline__ void norm_mod_row_f8(const float* xrow, const float* A, const float* B, unsigned char* orow, int lane) {
;     ...
;     const float rstd = 1.f / sqrtf(wave_sum(s) * (1.f / DM) + EPS_);
; #pragma unroll
;     for (int j = 0; j < 4; ++j) {
;         const f32x4 a0 = *(const f32x4*)((const char*)(A + 512 * j) + l32), a1 = *(const f32x4*)((const char*)(A + 512 * j + 4) + l32);
;         const f32x4 b0 = *(const f32x4*)((const char*)(B + 512 * j) + l32), b1 = *(const f32x4*)((const char*)(B + 512 * j + 4) + l32);
;         u32x2 q8; q8.x = pg8::pack4_fp8(v[2 * j] * rstd * a0 + b0, pg8::F8_SH); q8.y = pg8::pack4_fp8(v[2 * j + 1] * rstd * a1 + b1, pg8::F8_SH);
;         *(u32x2*)((char*)(orow + 512 * j) + l8) = q8; }
	v_add_f32_e32 v80, v80, v81
	v_fmamk_f32 v80, v80, 0x3a000000, v59
	v_mul_f32_e32 v81, 0x4f800000, v80
	v_cmp_gt_f32_e32 vcc, s9, v80
	s_nop 1
	v_cndmask_b32_e32 v80, v80, v81, vcc
	v_sqrt_f32_e32 v81, v80
	s_nop 0
	v_add_u32_e32 v82, -1, v81
	v_add_u32_e32 v83, 1, v81
	v_fma_f32 v84, -v82, v81, v80
	v_fma_f32 v85, -v83, v81, v80
	v_cmp_ge_f32_e64 s[4:5], 0, v84
	s_nop 1
	v_cndmask_b32_e64 v81, v81, v82, s[4:5]
	v_cmp_lt_f32_e64 s[4:5], 0, v85
	s_nop 1
	v_cndmask_b32_e64 v81, v81, v83, s[4:5]
	v_mul_f32_e32 v82, 0x37800000, v81
	v_cndmask_b32_e32 v81, v81, v82, vcc
	v_cmp_class_f32_e32 vcc, v80, v60
	s_nop 1
	v_cndmask_b32_e32 v80, v81, v80, vcc
	v_div_scale_f32 v81, s[4:5], v80, v80, 1.0
	v_rcp_f32_e32 v83, v81
	v_div_scale_f32 v82, vcc, 1.0, v80, 1.0
	v_fma_f32 v84, -v81, v83, 1.0
	v_fmac_f32_e32 v83, v84, v83
	v_mul_f32_e32 v84, v82, v83
	v_fma_f32 v85, -v81, v84, v82
	v_fmac_f32_e32 v84, v85, v83
	v_fma_f32 v81, -v81, v84, v82
	v_div_fmas_f32 v81, v81, v83, v84
	v_div_fixup_f32 v80, v81, v80, 1.0
	v_pk_mul_f32 v[30:31], v[30:31], v[80:81] op_sel_hi:[1,0]
	v_pk_mul_f32 v[26:27], v[26:27], v[80:81] op_sel_hi:[1,0]
	v_pk_fma_f32 v[30:31], v[120:121], v[30:31], v[128:129]
	v_pk_fma_f32 v[26:27], v[124:125], v[26:27], v[132:133]
	v_med3_f32 v30, v30, s14, v61
	v_med3_f32 v31, v31, s14, v61
	v_med3_f32 v26, v26, s14, v61
	v_med3_f32 v27, v27, s14, v61
	v_cvt_pk_fp8_f32 v78, v30, v31
	v_cvt_pk_fp8_f32 v79, v26, v27
	v_pk_mul_f32 v[32:33], v[32:33], v[80:81] op_sel_hi:[1,0]
	v_pk_mul_f32 v[28:29], v[28:29], v[80:81] op_sel_hi:[1,0]
	v_pk_fma_f32 v[32:33], v[122:123], v[32:33], v[130:131]
	v_pk_fma_f32 v[28:29], v[126:127], v[28:29], v[134:135]
	v_med3_f32 v32, v32, s14, v61
	v_med3_f32 v33, v33, s14, v61
	v_med3_f32 v28, v28, s14, v61
	v_med3_f32 v29, v29, s14, v61
	v_cvt_pk_fp8_f32 v78, v32, v33 op_sel:[0,0,1]
	v_cvt_pk_fp8_f32 v79, v28, v29 op_sel:[0,0,1]
	v_pk_mul_f32 v[18:19], v[18:19], v[80:81] op_sel_hi:[1,0]
	v_pk_mul_f32 v[22:23], v[22:23], v[80:81] op_sel_hi:[1,0]
	v_mov_b32_e32 v70, 0
	global_store_dwordx2 v[50:51], v[78:79], off
	v_mov_b32_e32 v71, 0
	v_pk_mul_f32 v[20:21], v[20:21], v[80:81] op_sel_hi:[1,0]
	v_pk_mul_f32 v[24:25], v[24:25], v[80:81] op_sel_hi:[1,0]
	v_pk_mul_f32 v[14:15], v[14:15], v[80:81] op_sel_hi:[1,0]
	v_pk_mul_f32 v[10:11], v[10:11], v[80:81] op_sel_hi:[1,0]
	v_pk_mul_f32 v[16:17], v[16:17], v[80:81] op_sel_hi:[1,0]
	v_pk_mul_f32 v[12:13], v[12:13], v[80:81] op_sel_hi:[1,0]
	v_pk_mul_f32 v[6:7], v[6:7], v[80:81] op_sel_hi:[1,0]
	v_pk_mul_f32 v[2:3], v[2:3], v[80:81] op_sel_hi:[1,0]
	v_pk_mul_f32 v[8:9], v[8:9], v[80:81] op_sel_hi:[1,0]
	v_pk_mul_f32 v[4:5], v[4:5], v[80:81] op_sel_hi:[1,0]
	v_pk_fma_f32 v[18:19], v[18:19], v[140:141], v[136:137]
	s_nop 0
	v_med3_f32 v18, v18, s14, v61
	v_pk_fma_f32 v[22:23], v[22:23], v[144:145], v[148:149]
	v_med3_f32 v19, v19, s14, v61
	v_med3_f32 v22, v22, s14, v61
	v_med3_f32 v23, v23, s14, v61
	v_cvt_pk_fp8_f32 v70, v18, v19
	v_cvt_pk_fp8_f32 v71, v22, v23
	v_pk_fma_f32 v[20:21], v[20:21], v[142:143], v[138:139]
	v_pk_fma_f32 v[24:25], v[24:25], v[146:147], v[150:151]
	v_med3_f32 v20, v20, s14, v61
	v_med3_f32 v21, v21, s14, v61
	v_med3_f32 v24, v24, s14, v61
	v_med3_f32 v25, v25, s14, v61
	v_cvt_pk_fp8_f32 v70, v20, v21 op_sel:[0,0,1]
	v_cvt_pk_fp8_f32 v71, v24, v25 op_sel:[0,0,1]
	v_mov_b32_e32 v62, 0
	v_mov_b32_e32 v63, 0
	global_store_dwordx2 v[50:51], v[70:71], off offset:512
	v_pk_fma_f32 v[14:15], v[14:15], v[156:157], v[152:153]
	s_nop 0
	v_med3_f32 v14, v14, s14, v61
	v_pk_fma_f32 v[10:11], v[10:11], v[160:161], v[164:165]
	v_med3_f32 v15, v15, s14, v61
	v_med3_f32 v10, v10, s14, v61
	v_med3_f32 v11, v11, s14, v61
	v_cvt_pk_fp8_f32 v62, v14, v15
	v_cvt_pk_fp8_f32 v63, v10, v11
	v_pk_fma_f32 v[16:17], v[16:17], v[158:159], v[154:155]
	v_pk_fma_f32 v[12:13], v[12:13], v[162:163], v[166:167]
	v_med3_f32 v16, v16, s14, v61
	v_med3_f32 v17, v17, s14, v61
	v_med3_f32 v12, v12, s14, v61
	v_med3_f32 v13, v13, s14, v61
	v_cvt_pk_fp8_f32 v62, v16, v17 op_sel:[0,0,1]
	v_cvt_pk_fp8_f32 v63, v12, v13 op_sel:[0,0,1]
	v_mov_b32_e32 v26, 0
	v_mov_b32_e32 v27, 0
	global_store_dwordx2 v[50:51], v[62:63], off offset:1024
	v_pk_fma_f32 v[6:7], v[6:7], v[172:173], v[168:169]
	s_nop 0
	v_med3_f32 v6, v6, s14, v61
	v_pk_fma_f32 v[2:3], v[2:3], v[176:177], v[180:181]
	v_med3_f32 v7, v7, s14, v61
	v_med3_f32 v2, v2, s14, v61
	v_med3_f32 v3, v3, s14, v61
	v_cvt_pk_fp8_f32 v26, v6, v7
	v_cvt_pk_fp8_f32 v27, v2, v3
	v_pk_fma_f32 v[8:9], v[8:9], v[174:175], v[170:171]
	v_pk_fma_f32 v[4:5], v[4:5], v[178:179], v[182:183]
	v_med3_f32 v8, v8, s14, v61
	v_med3_f32 v9, v9, s14, v61
	v_med3_f32 v4, v4, s14, v61
	v_med3_f32 v2, v5, s14, v61
	v_cvt_pk_fp8_f32 v26, v8, v9 op_sel:[0,0,1]
	v_cvt_pk_fp8_f32 v27, v4, v2 op_sel:[0,0,1]
	global_store_dwordx2 v[50:51], v[26:27], off offset:1536
	v_lshl_add_u64 v[50:51], v[50:51], 0, s[10:11]
	s_cbranch_scc1 .LBB0_201
